# converter class of P1 concentrated in XCDs 4-7 (workgroups >=128 with bit 2 set convert; those with bit 2 clear run the extra two GEMM units of id+4)
# baseline (speedup 1.0000x reference)
; #define LAS __attribute__((address_space(3)))
; template <class T> __device__ __forceinline__ T* opaque_p(T* p) { asm volatile("" : "+s"(p)); return p; }
; __device__ __forceinline__ int tidx(int wid) { int l; asm volatile("v_mbcnt_lo_u32_b32 %0, -1, 0\n\tv_mbcnt_hi_u32_b32 %0, -1, %0" : "=v"(l)); return (wid << 6) + l; }
; __device__ __forceinline__ int opaque_s(int v) { asm volatile("" : "+s"(v)); return v; }
;     __device__ bool next(int i, Unit& u) const {
;         const long L = (long)i * G + c; if (L >= nwg) return false;
;         int wgid = (int)L; { const int q = nwg / NXCD, r = nwg % NXCD, xcd = wgid % NXCD, off = wgid / NXCD; wgid = (xcd < r ? xcd * (q + 1) : r * (q + 1) + (xcd - r) * q) + off; }
;         const int nig = WGM * nN, gid = wgid / nig, fm = gid * WGM, gsz = (nM - fm) < WGM ? (nM - fm) : WGM;
;         u.pm = fm + ((wgid % nig) % gsz); u.pn = (wgid % nig) / gsz; u.aoff = (unsigned)u.pm * atile; u.boff = (unsigned)u.pn * btile; return true;
; __global__ void __launch_bounds__(NTHREADS, 2) hybrid_fwd(Args a) {
;     ...
;         if (PHEN(1) && IN(pb + 0)) for (int rep = 0; rep < NREP(1); ++rep) { unsigned char* ws = opaque_p(a.ws); LAS unsigned char* lds = opaque_p(lds0); const int bid = opaque_s((int)blockIdx.x); const int tid = tidx(wid0), lane = tid & 63, wave = __builtin_amdgcn_readfirstlane(tid >> 6), gw = bid * NWAVES + wave; (void)lane; (void)gw;
;             pg8::Gemm g{ws, (unsigned)WS_XB, (unsigned)(WS_WIN + (size_t)l * DIN * DM), DM / 2, DM / 2, opaque_s(DM / 2)};
;             pg8::GridOrder S; S.init(MTOK, DIN, DM / 2, DM / 2, G, bid);
;             EpiZ E{(bf16_t*)(ws + WS_Z), (const float*)(ws + WS_COS), (const float*)(ws + WS_SIN)};
;             pg8::gemm_phase<EpiZ, pg8::GridOrder, true, true>(lds, g, S, E, wid0);
.Lcg_setup:
	v_readlane_b32 s0, v255, 6
	v_readlane_b32 s2, v255, 8
	v_readlane_b32 s3, v255, 9
	s_mov_b64 s[4:5], s[2:3]
	s_mov_b32 s26, s93
	v_readlane_b32 s21, v255, 0
	v_readlane_b32 s6, v255, 61
	s_nop 0
	s_cmp_eq_u32 s6, 1
	s_cbranch_scc0 .Lcg_a
	s_addk_i32 s21, 0x4
.Lcg_a:
	s_movk_i32 s2, 0x400
	v_readlane_b32 s1, v255, 7
	v_mbcnt_lo_u32_b32 v172, -1, 0
	v_mbcnt_hi_u32_b32 v172, -1, v172
	s_waitcnt vmcnt(0)
	v_mbcnt_lo_u32_b32 v0, -1, 0
	v_mbcnt_hi_u32_b32 v0, -1, v0
	s_cmpk_lt_i32 s21, 0x280
	v_add_u32_e32 v173, s78, v172
	v_add_u32_e32 v1, s78, v0
	v_readfirstlane_b32 s20, v173
	s_cselect_b64 s[0:1], -1, 0
	v_readlane_b32 s6, v255, 61
	s_nop 0
	s_cmp_lg_u32 s6, 0
	s_cbranch_scc1 .Lcg_nodiv
	s_cmpk_lt_i32 s21, 0x80
	s_cbranch_scc1 .Lcg_nodiv
	s_bitcmp0_b32 s21, 2
	s_cbranch_scc1 .Lcg_nodiv
	s_cmp_eq_u32 s66, 3
	s_cbranch_scc1 .Lcg_nodiv
	v_writelane_b32 v255, 3, 61
	s_branch .LBB0_208

; #define LAS __attribute__((address_space(3)))
; template <class T> __device__ __forceinline__ T* opaque_p(T* p) { asm volatile("" : "+s"(p)); return p; }
; __device__ __forceinline__ int tidx(int wid) { int l; asm volatile("v_mbcnt_lo_u32_b32 %0, -1, 0\n\tv_mbcnt_hi_u32_b32 %0, -1, %0" : "=v"(l)); return (wid << 6) + l; }
; __device__ __forceinline__ int opaque_s(int v) { asm volatile("" : "+s"(v)); return v; }
; __global__ void __launch_bounds__(NTHREADS, 2) hybrid_fwd(Args a) {
;     ...
;         if (PHEN(1) && IN(pb + 0)) for (int rep = 0; rep < NREP(1); ++rep) { unsigned char* ws = opaque_p(a.ws); LAS unsigned char* lds = opaque_p(lds0); const int bid = opaque_s((int)blockIdx.x); const int tid = tidx(wid0), lane = tid & 63, wave = __builtin_amdgcn_readfirstlane(tid >> 6), gw = bid * NWAVES + wave; (void)lane; (void)gw;
;             pg8::Gemm g{ws, (unsigned)WS_XB, (unsigned)(WS_WIN + (size_t)l * DIN * DM), DM / 2, DM / 2, opaque_s(DM / 2)};
;             pg8::GridOrder S; S.init(MTOK, DIN, DM / 2, DM / 2, G, bid);
;             EpiZ E{(bf16_t*)(ws + WS_Z), (const float*)(ws + WS_COS), (const float*)(ws + WS_SIN)};
;             pg8::gemm_phase<EpiZ, pg8::GridOrder, true, true>(lds, g, S, E, wid0);
;             if (l + 1 < NLAYER && G == 256 && bid >= 128)
;                 f8_convert<true>(a, lds, ws, l + 1, 0, 0, 2, (unsigned*)(ws + WS_CTL) + CW_TICK + 64 * (l + 1), tid, lane, wave);
;         }
.Lcg_first:
	v_readlane_b32 s36, v255, 0
	s_nop 0
	s_cmpk_lt_i32 s36, 0x80
	s_cbranch_scc1 .Lcg_x
	s_bitcmp1_b32 s36, 2
	s_cbranch_scc1 .Lcg_x
	s_cmp_eq_u32 s66, 3
	s_cbranch_scc1 .Lcg_x
	v_writelane_b32 v255, 1, 61
	s_waitcnt vmcnt(0) lgkmcnt(0)
	s_barrier
	s_branch .Lcg_setup
